# v_pk_mov_b32 (12 sites in the RWKV chunk pass) also split into scalar moves; on top of v38
# speedup vs baseline: 1.0030x; 1.0030x over previous
.LBB0_1306:
	s_or_b64 exec, exec, s[0:1]
	v_add_f32_e32 v137, v153, v137
	v_sub_f32_e32 v136, v137, v136
	v_mul_f32_e32 v153, 0x3fb8aa3b, v137
	v_mul_f32_e32 v136, 0x3fb8aa3b, v136
	v_exp_f32_e32 v154, v153
	v_mul_f32_e32 v153, 0xbfb8aa3b, v137
	v_exp_f32_e32 v162, v136
	v_sub_f32_e32 v136, v152, v137
	v_add_f32_e32 v188, v157, v156
	v_add_f32_e32 v156, v135, v134
	v_exp_f32_e32 v159, v153
	v_mul_f32_e32 v136, 0x3fb8aa3b, v136
	v_mul_f32_e32 v134, 0x3fb8aa3b, v156
	v_lshl_add_u64 v[152:153], s[16:17], 0, v[142:143]
	v_exp_f32_e32 v160, v136
	v_exp_f32_e32 v157, v134
	global_load_dwordx4 v[134:137], v[152:153], off
	v_sub_f32_e32 v150, v156, v150
	v_mul_f32_e32 v150, 0x3fb8aa3b, v150
	v_add_f32_e32 v139, v141, v139
	v_exp_f32_e32 v171, v150
	v_sub_f32_e32 v150, v151, v156
	v_sub_f32_e32 v138, v139, v138
	v_mul_f32_e32 v150, 0x3fb8aa3b, v150
	v_mul_f32_e32 v141, 0x3fb8aa3b, v139
	v_mul_f32_e32 v138, 0x3fb8aa3b, v138
	v_mul_f32_e32 v158, 0xbfb8aa3b, v156
	v_exp_f32_e32 v165, v150
	v_exp_f32_e32 v156, v141
	v_mul_f32_e32 v141, 0xbfb8aa3b, v139
	v_exp_f32_e32 v170, v138
	v_sub_f32_e32 v138, v140, v139
	v_lshl_add_u64 v[150:151], s[18:19], 0, v[142:143]
	v_exp_f32_e32 v167, v141
	v_mul_f32_e32 v164, 0x3fb8aa3b, v138
	global_load_dwordx4 v[138:141], v[150:151], off
	v_add_f32_e32 v182, v169, v166
	v_sub_f32_e32 v131, v182, v131
	v_mul_f32_e32 v131, 0x3fb8aa3b, v131
	v_exp_f32_e32 v191, v131
	v_sub_f32_e32 v131, v175, v182
	v_mul_f32_e32 v131, 0x3fb8aa3b, v131
	v_exp_f32_e32 v175, v131
	v_add_f32_e32 v131, v177, v168
	v_mul_f32_e32 v168, 0x3fb8aa3b, v131
	v_mul_f32_e32 v177, 0xbfb8aa3b, v131
	v_sub_f32_e32 v174, v131, v174
	v_sub_f32_e32 v131, v176, v131
	v_mul_f32_e32 v174, 0x3fb8aa3b, v174
	v_mul_f32_e32 v131, 0x3fb8aa3b, v131
	v_exp_f32_e32 v190, v174
	v_exp_f32_e32 v174, v131
	v_add_f32_e32 v131, v173, v148
	v_mul_f32_e32 v148, 0x3fb8aa3b, v131
	v_sub_f32_e32 v130, v131, v130
	v_exp_f32_e32 v173, v148
	v_mul_f32_e32 v148, 0xbfb8aa3b, v131
	v_mul_f32_e32 v130, 0x3fb8aa3b, v130
	v_mul_f32_e32 v166, 0x3fb8aa3b, v182
	v_exp_f32_e32 v176, v148
	v_exp_f32_e32 v187, v130
	v_sub_f32_e32 v130, v149, v131
	v_lshl_add_u64 v[148:149], s[20:21], 0, v[142:143]
	v_exp_f32_e32 v169, v166
	v_mul_f32_e32 v166, 0xbfb8aa3b, v182
	global_load_dwordx4 v[182:185], v[148:149], off
	v_mul_f32_e32 v130, 0x3fb8aa3b, v130
	v_exp_f32_e32 v195, v130
	v_add_f32_e32 v130, v172, v161
	v_mul_f32_e32 v131, 0x3fb8aa3b, v130
	v_exp_f32_e32 v172, v131
	v_mul_f32_e32 v131, 0xbfb8aa3b, v130
	v_exp_f32_e32 v196, v131
	v_sub_f32_e32 v131, v130, v155
	v_sub_f32_e32 v130, v163, v130
	v_mul_f32_e32 v130, 0x3fb8aa3b, v130
	v_exp_f32_e32 v194, v130
	v_mul_f32_e32 v130, 0x3fb8aa3b, v188
	v_exp_f32_e32 v155, v130
	v_mul_f32_e32 v130, 0xbfb8aa3b, v188
	v_exp_f32_e32 v198, v130
	v_sub_f32_e32 v130, v188, v132
	v_mul_f32_e32 v130, 0x3fb8aa3b, v130
	v_mul_f32_e32 v131, 0x3fb8aa3b, v131
	v_exp_f32_e32 v163, v130
	v_sub_f32_e32 v130, v133, v188
	v_exp_f32_e32 v186, v131
	v_mul_f32_e32 v161, 0x3fb8aa3b, v130
	global_load_dwordx4 v[130:133], v[146:147], off offset:16
	v_lshl_add_u64 v[142:143], s[22:23], 0, v[142:143]
	v_or_b32_e32 v197, v180, v178
	v_exp_f32_e32 v177, v177
	v_exp_f32_e32 v166, v166
	v_exp_f32_e32 v164, v164
	v_exp_f32_e32 v158, v158
	v_exp_f32_e32 v161, v161
	s_waitcnt vmcnt(3)
	v_cvt_f32_f16_e32 v146, v134
	v_cvt_f32_f16_sdwa v147, v134 dst_sel:DWORD dst_unused:UNUSED_PAD src0_sel:WORD_1
	v_cvt_f32_f16_e32 v192, v135
	v_cvt_f32_f16_sdwa v193, v135 dst_sel:DWORD dst_unused:UNUSED_PAD src0_sel:WORD_1
	v_exp_f32_e32 v168, v168
	v_mul_f32_e32 v134, v186, v146
	v_mul_f32_e32 v135, v187, v147
	global_load_dwordx4 v[186:189], v[142:143], off
	v_mul_f32_e32 v146, v190, v192
	v_mul_f32_e32 v147, v191, v193
	v_cvt_f32_f16_e32 v190, v136
	v_cvt_f32_f16_sdwa v191, v136 dst_sel:DWORD dst_unused:UNUSED_PAD src0_sel:WORD_1
	v_cvt_f32_f16_e32 v192, v137
	v_cvt_f32_f16_sdwa v193, v137 dst_sel:DWORD dst_unused:UNUSED_PAD src0_sel:WORD_1
	v_cvt_pk_f16_f32 v134, v134, v135
	v_cvt_pk_f16_f32 v135, v146, v147
	v_mul_f32_e32 v136, v170, v190
	v_mul_f32_e32 v137, v171, v191
	v_mul_f32_e32 v146, v162, v192
	v_mul_f32_e32 v147, v163, v193
	v_cvt_pk_f16_f32 v136, v136, v137
	v_cvt_pk_f16_f32 v137, v146, v147
	v_add_u32_e32 v147, s36, v197
	ds_write_b128 v147, v[134:137]
	s_waitcnt vmcnt(3)
	v_cvt_f32_f16_e32 v136, v138
	v_cvt_f32_f16_sdwa v137, v138 dst_sel:DWORD dst_unused:UNUSED_PAD src0_sel:WORD_1
	v_cvt_f32_f16_e32 v162, v139
	v_cvt_f32_f16_sdwa v163, v139 dst_sel:DWORD dst_unused:UNUSED_PAD src0_sel:WORD_1
	v_fma_mixlo_f16 v146, v196, v138, 0 op_sel_hi:[0,1,0]
	v_cvt_f32_f16_e32 v138, v140
	v_cvt_f32_f16_sdwa v139, v140 dst_sel:DWORD dst_unused:UNUSED_PAD src0_sel:WORD_1
	v_mul_f32_e32 v134, v194, v136
	v_mul_f32_e32 v135, v195, v137
	v_mov_b32_e32 v136, v137
	v_mov_b32_e32 v137, v162
	v_cvt_pk_f16_f32 v134, v134, v135
	v_mul_f32_e32 v136, v176, v136
	v_mul_f32_e32 v137, v177, v137
	s_nop 0
	v_cvt_pk_f16_f32 v170, v136, v137
	v_mul_f32_e32 v136, v174, v162
	v_mul_f32_e32 v137, v175, v163
	v_pack_b32_f16 v190, v146, v170
	v_cvt_pk_f16_f32 v135, v136, v137
	v_mov_b32_e32 v136, v163
	v_mov_b32_e32 v137, v138
	v_cvt_f32_f16_e32 v162, v141
	v_cvt_f32_f16_sdwa v163, v141 dst_sel:DWORD dst_unused:UNUSED_PAD src0_sel:WORD_1
	v_mul_f32_e32 v136, v166, v136
	v_mul_f32_e32 v137, v167, v137
	s_nop 0
	v_cvt_pk_f16_f32 v140, v136, v137
	v_mul_f32_e32 v136, v164, v138
	v_mul_f32_e32 v137, v165, v139
	v_mov_b32_e32 v138, v139
	v_mov_b32_e32 v139, v162
	v_cvt_pk_f16_f32 v136, v136, v137
	v_mul_f32_e32 v138, v158, v138
	v_mul_f32_e32 v139, v159, v139
	v_alignbit_b32 v191, v140, v170, 16
	v_cvt_pk_f16_f32 v137, v138, v139
	v_lshrrev_b32_e32 v193, 16, v137
	v_mul_f32_e32 v138, v160, v162
	v_mul_f32_e32 v139, v161, v163
	v_alignbit_b32 v192, v137, v140, 16
	v_cvt_pk_f16_f32 v137, v138, v139
	v_fma_mixhi_f16 v193, v198, v141, 0 op_sel:[0,1,0] op_sel_hi:[0,1,0]
	ds_write_b128 v147, v[190:193] offset:2048
	ds_write_b128 v147, v[134:137] offset:8192
	s_waitcnt vmcnt(2)
	v_cvt_f32_f16_e32 v136, v182
	v_cvt_f32_f16_sdwa v137, v182 dst_sel:DWORD dst_unused:UNUSED_PAD src0_sel:WORD_1
	v_cvt_f32_f16_e32 v140, v183
	v_cvt_f32_f16_sdwa v141, v183 dst_sel:DWORD dst_unused:UNUSED_PAD src0_sel:WORD_1
	v_cvt_f32_f16_e32 v162, v184
	v_cvt_f32_f16_sdwa v163, v184 dst_sel:DWORD dst_unused:UNUSED_PAD src0_sel:WORD_1
	v_mul_f32_e32 v134, v194, v136
	v_mul_f32_e32 v135, v195, v137
	v_mov_b32_e32 v136, v137
	v_mov_b32_e32 v137, v140
	v_cvt_pk_f16_f32 v134, v134, v135
	v_mul_f32_e32 v136, v176, v136
	v_mul_f32_e32 v137, v177, v137
	v_fma_mixlo_f16 v138, v196, v182, 0 op_sel_hi:[0,1,0]
	v_cvt_pk_f16_f32 v139, v136, v137
	v_mul_f32_e32 v136, v174, v140
	v_mul_f32_e32 v137, v175, v141
	v_pack_b32_f16 v138, v138, v139
	v_cvt_pk_f16_f32 v135, v136, v137
	v_mov_b32_e32 v136, v141
	v_mov_b32_e32 v137, v162
	s_nop 0
	v_mul_f32_e32 v136, v166, v136
	v_mul_f32_e32 v137, v167, v137
	v_cvt_f32_f16_e32 v166, v185
	v_cvt_f32_f16_sdwa v167, v185 dst_sel:DWORD dst_unused:UNUSED_PAD src0_sel:WORD_1
	v_cvt_pk_f16_f32 v146, v136, v137
	v_mul_f32_e32 v136, v164, v162
	v_mul_f32_e32 v137, v165, v163
	v_alignbit_b32 v139, v146, v139, 16
	v_mov_b32_e32 v140, v163
	v_mov_b32_e32 v141, v166
	v_cvt_pk_f16_f32 v136, v136, v137
	v_mul_f32_e32 v140, v158, v140
	v_mul_f32_e32 v141, v159, v141
	v_mul_f32_e32 v158, v160, v166
	v_mul_f32_e32 v159, v161, v167
	v_cvt_pk_f16_f32 v137, v140, v141
	v_lshrrev_b32_e32 v141, 16, v137
	v_alignbit_b32 v140, v137, v146, 16
	v_fma_mixhi_f16 v141, v198, v185, 0 op_sel:[0,1,0] op_sel_hi:[0,1,0]
	ds_write_b128 v147, v[138:141] offset:4096
	s_waitcnt vmcnt(0)
	v_cvt_f32_f16_e32 v138, v186
	v_cvt_f32_f16_sdwa v139, v186 dst_sel:DWORD dst_unused:UNUSED_PAD src0_sel:WORD_1
	v_cvt_pk_f16_f32 v137, v158, v159
	v_cvt_f32_f16_e32 v140, v187
	v_cvt_f32_f16_sdwa v141, v187 dst_sel:DWORD dst_unused:UNUSED_PAD src0_sel:WORD_1
	ds_write_b128 v147, v[134:137] offset:10240
	v_cvt_f32_f16_e32 v136, v188
	v_cvt_f32_f16_sdwa v137, v188 dst_sel:DWORD dst_unused:UNUSED_PAD src0_sel:WORD_1
	v_mul_f32_e32 v134, v172, v138
	v_mul_f32_e32 v135, v173, v139
	v_mul_f32_e32 v136, v156, v136
	v_mul_f32_e32 v137, v157, v137
	v_cvt_pk_f16_f32 v138, v134, v135
	v_mul_f32_e32 v134, v168, v140
	v_mul_f32_e32 v135, v169, v141
	v_cvt_pk_f16_f32 v140, v136, v137
	v_cvt_pk_f16_f32 v139, v134, v135
	v_cvt_f32_f16_e32 v134, v189
	v_cvt_f32_f16_sdwa v135, v189 dst_sel:DWORD dst_unused:UNUSED_PAD src0_sel:WORD_1
	v_cvt_f32_f16_e32 v137, v130
	v_mul_f32_e32 v134, v154, v134
	v_mul_f32_e32 v135, v155, v135
	s_nop 0
	v_cvt_pk_f16_f32 v141, v134, v135
	v_add_f32_dpp v134, v137, v137 row_shr:1 row_mask:0xf bank_mask:0xf bound_ctrl:1
	ds_write_b128 v147, v[138:141] offset:6144
	v_mov_b32_e32 v154, 0
	v_add_f32_dpp v134, v134, v134 row_shr:2 row_mask:0xf bank_mask:0xf bound_ctrl:1
	s_nop 1
	v_add_f32_dpp v139, v134, v134 row_shr:4 row_mask:0xf bank_mask:0xf bound_ctrl:1
	v_add_f32_dpp v134, v137, v137 quad_perm:[1,0,3,2] row_mask:0xf bank_mask:0xf bound_ctrl:1
	s_nop 0
	v_mov_b32_dpp v154, v139 row_shr:8 row_mask:0xf bank_mask:0xf
	v_add_f32_dpp v134, v134, v134 quad_perm:[2,3,0,1] row_mask:0xf bank_mask:0xf bound_ctrl:1
	s_nop 1
	v_add_f32_dpp v134, v134, v134 row_half_mirror row_mask:0xf bank_mask:0xf bound_ctrl:1
	s_nop 1
	v_add_f32_dpp v155, v134, v134 row_mirror row_mask:0xf bank_mask:0xf bound_ctrl:1
	s_and_saveexec_b64 s[0:1], vcc
	s_cbranch_execz .LBB0_1308
	v_mul_f32_e32 v134, 0x3fb8aa3b, v155
	v_exp_f32_e32 v134, v134
	ds_write_b32 v181, v134 offset:16416

.LBB0_1322:
	s_or_b64 exec, exec, s[0:1]
	v_add_f32_e32 v174, v174, v130
	v_mul_f32_e32 v130, 0x3fb8aa3b, v174
	v_mul_f32_e32 v133, 0xbfb8aa3b, v174
	v_sub_f32_e32 v136, v174, v136
	v_sub_f32_e32 v138, v138, v174
	global_load_dwordx4 v[174:177], v[152:153], off offset:16
	v_add_f32_e32 v152, v135, v132
	v_sub_f32_e32 v141, v152, v141
	v_mul_f32_e32 v132, 0x3fb8aa3b, v152
	v_mul_f32_e32 v141, 0x3fb8aa3b, v141
	v_add_f32_e32 v181, v173, v172
	v_exp_f32_e32 v135, v132
	v_mul_f32_e32 v132, 0xbfb8aa3b, v152
	v_exp_f32_e32 v183, v141
	v_sub_f32_e32 v141, v171, v152
	v_add_f32_e32 v152, v170, v134
	global_load_dwordx4 v[170:173], v[150:151], off offset:16
	v_add_f32_e32 v150, v167, v165
	v_sub_f32_e32 v131, v150, v131
	v_mul_f32_e32 v131, 0x3fb8aa3b, v131
	v_exp_f32_e32 v167, v131
	v_sub_f32_e32 v131, v166, v150
	v_sub_f32_e32 v140, v152, v140
	v_mul_f32_e32 v131, 0x3fb8aa3b, v131
	v_mul_f32_e32 v140, 0x3fb8aa3b, v140
	v_exp_f32_e32 v185, v131
	v_add_f32_e32 v131, v163, v161
	v_mul_f32_e32 v134, 0x3fb8aa3b, v152
	v_mul_f32_e32 v153, 0xbfb8aa3b, v152
	v_exp_f32_e32 v182, v140
	v_sub_f32_e32 v140, v169, v152
	v_mul_f32_e32 v151, 0x3fb8aa3b, v150
	v_mul_f32_e32 v152, 0xbfb8aa3b, v150
	v_mul_f32_e32 v150, 0x3fb8aa3b, v131
	v_mul_f32_e32 v161, 0xbfb8aa3b, v131
	v_sub_f32_e32 v160, v131, v160
	v_sub_f32_e32 v131, v162, v131
	v_mul_f32_e32 v131, 0x3fb8aa3b, v131
	v_exp_f32_e32 v184, v131
	v_add_f32_e32 v131, v159, v158
	v_mul_f32_e32 v160, 0x3fb8aa3b, v160
	v_mul_f32_e32 v158, 0x3fb8aa3b, v131
	v_exp_f32_e32 v187, v161
	v_exp_f32_e32 v166, v160
	v_exp_f32_e32 v189, v158
	global_load_dwordx4 v[158:161], v[148:149], off offset:16
	v_mul_f32_e32 v162, 0xbfb8aa3b, v131
	v_sub_f32_e32 v148, v131, v156
	v_sub_f32_e32 v131, v157, v131
	v_mul_f32_e32 v131, 0x3fb8aa3b, v131
	v_exp_f32_e32 v191, v131
	v_add_f32_e32 v131, v139, v154
	v_mul_f32_e32 v139, 0x3fb8aa3b, v131
	v_exp_f32_e32 v188, v139
	v_mul_f32_e32 v139, 0xbfb8aa3b, v131
	v_sub_f32_e32 v137, v131, v137
	v_sub_f32_e32 v131, v155, v131
	global_load_dwordx4 v[154:157], v[142:143], off offset:16
	v_mul_f32_e32 v148, 0x3fb8aa3b, v148
	v_mul_f32_e32 v137, 0x3fb8aa3b, v137
	v_exp_f32_e32 v186, v162
	v_exp_f32_e32 v149, v148
	v_exp_f32_e32 v148, v137
	v_mul_f32_e32 v137, 0xbfb8aa3b, v181
	v_exp_f32_e32 v193, v137
	v_sub_f32_e32 v137, v181, v164
	v_mul_f32_e32 v136, 0x3fb8aa3b, v136
	v_mul_f32_e32 v137, 0x3fb8aa3b, v137
	v_exp_f32_e32 v136, v136
	v_exp_f32_e32 v137, v137
	v_mul_f32_e32 v131, 0x3fb8aa3b, v131
	v_exp_f32_e32 v190, v131
	v_exp_f32_e32 v153, v153
	v_exp_f32_e32 v152, v152
	v_mul_f32_e32 v141, 0x3fb8aa3b, v141
	v_mul_f32_e32 v140, 0x3fb8aa3b, v140
	v_exp_f32_e32 v192, v139
	v_exp_f32_e32 v141, v141
	v_exp_f32_e32 v140, v140
	v_exp_f32_e32 v133, v133
	v_exp_f32_e32 v132, v132
	v_sub_f32_e32 v139, v168, v181
	v_mul_f32_e32 v138, 0x3fb8aa3b, v138
	v_mul_f32_e32 v139, 0x3fb8aa3b, v139
	v_exp_f32_e32 v138, v138
	s_waitcnt vmcnt(3)
	v_cvt_f32_f16_sdwa v163, v174 dst_sel:DWORD dst_unused:UNUSED_PAD src0_sel:WORD_1
	v_cvt_f32_f16_e32 v162, v174
	v_cvt_f32_f16_sdwa v165, v175 dst_sel:DWORD dst_unused:UNUSED_PAD src0_sel:WORD_1
	v_cvt_f32_f16_e32 v164, v175
	v_exp_f32_e32 v139, v139
	v_mul_f32_e32 v142, v148, v162
	v_mul_f32_e32 v143, v149, v163
	v_cvt_f32_f16_sdwa v149, v176 dst_sel:DWORD dst_unused:UNUSED_PAD src0_sel:WORD_1
	v_cvt_pk_f16_f32 v162, v142, v143
	v_mul_f32_e32 v142, v166, v164
	v_mul_f32_e32 v143, v167, v165
	v_cvt_f32_f16_e32 v148, v176
	v_cvt_f32_f16_sdwa v167, v177 dst_sel:DWORD dst_unused:UNUSED_PAD src0_sel:WORD_1
	v_cvt_f32_f16_e32 v166, v177
	v_cvt_pk_f16_f32 v163, v142, v143
	v_mul_f32_e32 v142, v182, v148
	v_mul_f32_e32 v143, v183, v149
	v_mul_f32_e32 v131, 0x3fb8aa3b, v181
	v_mul_f32_e32 v136, v136, v166
	v_mul_f32_e32 v137, v137, v167
	v_cvt_pk_f16_f32 v164, v142, v143
	v_cvt_pk_f16_f32 v165, v136, v137
	s_waitcnt vmcnt(2)
	v_cvt_f32_f16_sdwa v137, v170 dst_sel:DWORD dst_unused:UNUSED_PAD src0_sel:WORD_1
	v_cvt_f32_f16_e32 v136, v170
	v_cvt_f32_f16_sdwa v143, v171 dst_sel:DWORD dst_unused:UNUSED_PAD src0_sel:WORD_1
	v_cvt_f32_f16_e32 v142, v171
	ds_write_b128 v147, v[162:165] offset:16
	v_mul_f32_e32 v148, v190, v136
	v_mul_f32_e32 v149, v191, v137
	v_fma_mixlo_f16 v163, v192, v170, 0 op_sel_hi:[0,1,0]
	v_mov_b32_e32 v136, v137
	v_mov_b32_e32 v137, v142
	v_cvt_pk_f16_f32 v162, v148, v149
	v_mul_f32_e32 v136, v186, v136
	v_mul_f32_e32 v137, v187, v137
	v_mul_f32_e32 v148, v184, v142
	v_mul_f32_e32 v149, v185, v143
	v_cvt_pk_f16_f32 v164, v136, v137
	v_cvt_f32_f16_sdwa v137, v172 dst_sel:DWORD dst_unused:UNUSED_PAD src0_sel:WORD_1
	v_cvt_f32_f16_e32 v136, v172
	v_pack_b32_f16 v166, v163, v164
	v_cvt_pk_f16_f32 v163, v148, v149
	v_exp_f32_e32 v130, v130
	v_mov_b32_e32 v142, v143
	v_mov_b32_e32 v143, v136
	v_mul_f32_e32 v148, v140, v136
	v_mul_f32_e32 v149, v141, v137
	v_mul_f32_e32 v142, v152, v142
	v_mul_f32_e32 v143, v153, v143
	v_exp_f32_e32 v134, v134
	v_cvt_pk_f16_f32 v165, v142, v143
	v_cvt_f32_f16_sdwa v143, v173 dst_sel:DWORD dst_unused:UNUSED_PAD src0_sel:WORD_1
	v_cvt_f32_f16_e32 v142, v173
	v_alignbit_b32 v167, v165, v164, 16
	v_cvt_pk_f16_f32 v164, v148, v149
	v_exp_f32_e32 v151, v151
	v_mov_b32_e32 v136, v137
	v_mov_b32_e32 v137, v142
	v_exp_f32_e32 v150, v150
	v_mul_f32_e32 v136, v132, v136
	v_mul_f32_e32 v137, v133, v137
	v_exp_f32_e32 v131, v131
	v_cvt_pk_f16_f32 v136, v136, v137
	v_alignbit_b32 v168, v136, v165, 16
	v_lshrrev_b32_e32 v169, 16, v136
	v_mul_f32_e32 v136, v138, v142
	v_mul_f32_e32 v137, v139, v143
	s_waitcnt vmcnt(1)
	v_cvt_f32_f16_sdwa v143, v159 dst_sel:DWORD dst_unused:UNUSED_PAD src0_sel:WORD_1
	v_cvt_pk_f16_f32 v165, v136, v137
	v_cvt_f32_f16_sdwa v137, v158 dst_sel:DWORD dst_unused:UNUSED_PAD src0_sel:WORD_1
	v_cvt_f32_f16_e32 v136, v158
	v_cvt_f32_f16_e32 v142, v159
	v_fma_mixhi_f16 v169, v193, v173, 0 op_sel:[0,1,0] op_sel_hi:[0,1,0]
	ds_write_b128 v147, v[166:169] offset:2064
	ds_write_b128 v147, v[162:165] offset:8208
	v_mul_f32_e32 v148, v190, v136
	v_mul_f32_e32 v149, v191, v137
	v_mov_b32_e32 v136, v137
	v_mov_b32_e32 v137, v142
	v_cvt_pk_f16_f32 v162, v148, v149
	v_mul_f32_e32 v136, v186, v136
	v_mul_f32_e32 v137, v187, v137
	v_mul_f32_e32 v148, v184, v142
	v_mul_f32_e32 v149, v185, v143
	v_cvt_pk_f16_f32 v159, v136, v137
	v_cvt_f32_f16_sdwa v137, v160 dst_sel:DWORD dst_unused:UNUSED_PAD src0_sel:WORD_1
	v_cvt_f32_f16_e32 v136, v160
	v_cvt_pk_f16_f32 v163, v148, v149
	v_fma_mixlo_f16 v158, v192, v158, 0 op_sel_hi:[0,1,0]
	v_lshlrev_b32_e32 v213, 4, v212
	v_mov_b32_e32 v142, v143
	v_mov_b32_e32 v143, v136
	v_mul_f32_e32 v140, v140, v136
	v_mul_f32_e32 v141, v141, v137
	v_mul_f32_e32 v142, v152, v142
	v_mul_f32_e32 v143, v153, v143
	v_cvt_pk_f16_f32 v164, v140, v141
	v_cvt_pk_f16_f32 v148, v142, v143
	v_cvt_f32_f16_sdwa v143, v161 dst_sel:DWORD dst_unused:UNUSED_PAD src0_sel:WORD_1
	v_cvt_f32_f16_e32 v142, v161
	s_waitcnt vmcnt(0)
	v_cvt_f32_f16_sdwa v141, v157 dst_sel:DWORD dst_unused:UNUSED_PAD src0_sel:WORD_1
	v_cvt_f32_f16_e32 v140, v157
	v_pack_b32_f16 v166, v158, v159
	v_mov_b32_e32 v136, v137
	v_mov_b32_e32 v137, v142
	v_alignbit_b32 v167, v148, v159, 16
	v_mul_f32_e32 v132, v132, v136
	v_mul_f32_e32 v133, v133, v137
	v_cvt_f32_f16_sdwa v137, v155 dst_sel:DWORD dst_unused:UNUSED_PAD src0_sel:WORD_1
	v_cvt_pk_f16_f32 v132, v132, v133
	v_alignbit_b32 v168, v132, v148, 16
	v_lshrrev_b32_e32 v169, 16, v132
	v_mul_f32_e32 v132, v138, v142
	v_mul_f32_e32 v133, v139, v143
	v_cvt_f32_f16_e32 v136, v155
	v_cvt_pk_f16_f32 v165, v132, v133
	v_cvt_f32_f16_sdwa v133, v154 dst_sel:DWORD dst_unused:UNUSED_PAD src0_sel:WORD_1
	v_cvt_f32_f16_e32 v132, v154
	v_cvt_f32_f16_sdwa v139, v156 dst_sel:DWORD dst_unused:UNUSED_PAD src0_sel:WORD_1
	v_cvt_f32_f16_e32 v138, v156
	v_mul_f32_e32 v136, v150, v136
	v_mul_f32_e32 v137, v151, v137
	v_mul_f32_e32 v132, v188, v132
	v_mul_f32_e32 v133, v189, v133
	v_mul_f32_e32 v130, v130, v140
	v_mul_f32_e32 v131, v131, v141
	v_mul_f32_e32 v134, v134, v138
	v_mul_f32_e32 v135, v135, v139
	v_fma_mixhi_f16 v169, v193, v161, 0 op_sel:[0,1,0] op_sel_hi:[0,1,0]
	v_cvt_pk_f16_f32 v132, v132, v133
	v_cvt_pk_f16_f32 v133, v136, v137
	v_cvt_pk_f16_f32 v134, v134, v135
	v_cvt_pk_f16_f32 v135, v130, v131
	v_and_b32_e32 v130, 0xfffffe00, v213
	v_and_b32_e32 v131, 16, v212
	ds_write_b128 v147, v[166:169] offset:4112
	ds_write_b128 v147, v[162:165] offset:10256
	ds_write_b128 v147, v[132:135] offset:6160
	v_or3_b32 v130, v130, v131, v180
	s_waitcnt lgkmcnt(0)
	v_add_u32_e32 v142, s36, v130
	ds_read_b128 v[130:133], v142
	ds_read_b128 v[134:137], v142 offset:2048
	ds_read_b128 v[138:141], v142 offset:1024
	ds_read_b128 v[148:151], v142 offset:3072
	ds_read_b128 v[156:159], v142 offset:4096
	ds_read_b128 v[160:163], v142 offset:5120
	ds_read_b128 v[164:167], v142 offset:6144
	ds_read_b128 v[168:171], v142 offset:7168
	s_waitcnt lgkmcnt(6)
	v_mfma_f32_16x16x32_f16 v[152:155], v[130:133], v[134:137], 0
	v_lshlrev_b32_e32 v208, 2, v179
	v_lshl_add_u32 v215, v144, 2, s36
	v_cmp_gt_i32_e32 vcc, v208, v144
	s_waitcnt lgkmcnt(3)
	v_mfma_f32_16x16x32_f16 v[130:133], v[130:133], v[156:159], 0
	v_lshl_add_u32 v143, v179, 8, v215
	v_or_b32_e32 v211, 1, v208
	v_or_b32_e32 v209, 2, v208
	s_waitcnt lgkmcnt(1)
	v_mfma_f32_16x16x32_f16 v[134:137], v[164:167], v[134:137], 0
	v_or_b32_e32 v210, 3, v208
	v_mfma_f32_16x16x32_f16 v[156:159], v[164:167], v[156:159], 0
	v_mfma_f32_16x16x32_f16 v[130:133], v[138:141], v[160:163], v[130:133]
	v_mfma_f32_16x16x32_f16 v[152:155], v[138:141], v[148:151], v[152:155]
	s_waitcnt lgkmcnt(0)
	v_mfma_f32_16x16x32_f16 v[134:137], v[168:171], v[148:151], v[134:137]
	s_nop 4
	v_cvt_f16_f32_e32 v130, v130
	v_cvt_f16_f32_e32 v131, v131
	v_cndmask_b32_e32 v142, 0, v152, vcc
	v_mfma_f32_16x16x32_f16 v[138:141], v[168:171], v[160:163], v[156:159]
	v_cndmask_b32_e32 v130, 0, v130, vcc
	v_cvt_f16_f32_e32 v134, v134
	v_cvt_f16_f32_e32 v135, v135
	v_cmp_lt_i32_e32 vcc, v208, v144
	ds_write_b32 v143, v142 offset:14336
	s_nop 2
	v_cvt_f16_f32_e32 v138, v138
	v_cvt_f16_f32_e32 v139, v139
	v_cndmask_b32_e64 v142, v153, 0, vcc
	v_lshl_add_u32 v143, v211, 6, v215
	v_cndmask_b32_e64 v134, v134, 0, vcc
	v_cndmask_b32_e64 v138, v138, 0, vcc
	ds_write_b32 v143, v142 offset:14336
	v_cndmask_b32_e64 v142, v131, 0, vcc
	v_cmp_lt_i32_e32 vcc, v211, v144
	v_lshl_add_u32 v143, v209, 6, v215
	v_cvt_f16_f32_e32 v132, v132
	v_cndmask_b32_e64 v135, v135, 0, vcc
	v_cndmask_b32_e64 v139, v139, 0, vcc
	v_cmp_gt_i32_e32 vcc, v209, v144
	v_add_u32_e32 v161, s36, v180
	v_pack_b32_f16 v130, v130, v142
	v_cndmask_b32_e32 v131, 0, v154, vcc
	ds_write_b32 v143, v131 offset:14336
	v_cvt_f16_f32_e32 v131, v136
	v_cvt_f16_f32_e32 v136, v140
	v_cndmask_b32_e32 v132, 0, v132, vcc
	v_cmp_lt_i32_e32 vcc, v209, v144
	v_lshl_add_u32 v143, v210, 6, v215
	s_nop 0
	v_cndmask_b32_e64 v140, v131, 0, vcc
	v_cvt_f16_f32_e32 v131, v133
	v_cndmask_b32_e64 v136, v136, 0, vcc
	v_cmp_gt_i32_e32 vcc, v210, v144
	s_nop 1
	v_cndmask_b32_e32 v131, 0, v131, vcc
	v_pack_b32_f16 v131, v132, v131
	v_cvt_f16_f32_e32 v132, v137
	v_cvt_f16_f32_e32 v137, v141
	v_cndmask_b32_e32 v133, 0, v155, vcc
	v_cmp_lt_i32_e32 vcc, v210, v144
	ds_write_b32 v143, v133 offset:14336
	s_nop 0
	v_cndmask_b32_e64 v132, v132, 0, vcc
	v_pack_b32_f16 v133, v140, v132
	v_pack_b32_f16 v132, v134, v135
	v_cndmask_b32_e64 v134, v137, 0, vcc
	v_pack_b32_f16 v135, v136, v134
	v_lshlrev_b32_e32 v136, 3, v179
	v_add_u32_e32 v160, v161, v136
	v_pack_b32_f16 v134, v138, v139
	ds_write_b64 v160, v[130:131] offset:15872
	ds_write2st64_b64 v160, v[132:133], v[134:135] offset0:4 offset1:5
	s_waitcnt lgkmcnt(0)
	v_cmp_gt_u32_e32 vcc, 16, v212
	s_and_saveexec_b64 s[0:1], vcc
	s_cbranch_execz .LBB0_1289
	v_mov_b32_e32 v179, s36
	v_add_u32_e32 v214, 0x3800, v179
	ds_read2_b64 v[150:153], v214 offset0:8 offset1:16
	ds_read_b128 v[130:133], v179 offset:14528
	ds_read_b128 v[154:157], v179 offset:14592
	v_cmp_eq_u32_e32 vcc, 0, v144
	s_waitcnt lgkmcnt(2)
	v_mov_b32_e32 v136, v152
	v_cndmask_b32_e64 v148, 0, 1.0, vcc
	v_cmp_eq_u32_e32 vcc, 3, v144
	v_mov_b32_e32 v137, v150
	s_waitcnt lgkmcnt(1)
	v_mov_b32_e32 v158, v131
	v_cndmask_b32_e64 v133, 0, 1.0, vcc
	v_cmp_eq_u32_e32 vcc, 1, v144
	v_fma_f32 v147, -v148, v130, v133
	v_mov_b32_e32 v159, v132
	v_cndmask_b32_e64 v135, 0, 1.0, vcc
	v_cmp_eq_u32_e32 vcc, 2, v144
	s_waitcnt lgkmcnt(0)
	v_mov_b32_e32 v175, v154
	v_mov_b32_e32 v205, v156
	v_cndmask_b32_e64 v134, 0, 1.0, vcc
	v_fma_f32 v150, -v148, v136, v134
	v_fma_f32 v151, -v148, v137, v135
	ds_read_b128 v[140:143], v179 offset:15296
	ds_read_b128 v[136:139], v179 offset:15312
	ds_read_b128 v[162:165], v179 offset:14656
	ds_read_b128 v[130:133], v179 offset:14720
	ds_read_b128 v[166:169], v179 offset:14784
	ds_read_b128 v[170:173], v179 offset:14800
	v_cmp_eq_u32_e32 vcc, 4, v144
	s_waitcnt lgkmcnt(3)
	v_mov_b32_e32 v207, v164
	s_waitcnt lgkmcnt(2)
	v_mov_b32_e32 v206, v132
	v_cndmask_b32_e64 v135, 0, 1.0, vcc
	v_cmp_eq_u32_e32 vcc, 7, v144
	s_waitcnt lgkmcnt(1)
	v_mov_b32_e32 v174, v166
	v_mov_b32_e32 v154, v167
	v_cndmask_b32_e64 v134, 0, 1.0, vcc
	v_fma_f32 v134, -v148, v174, v134
	v_fma_f32 v135, -v148, v175, v135
	v_mov_b32_e32 v204, v168
	v_mov_b32_e32 v156, v169
	v_cmp_eq_u32_e32 vcc, 5, v144
	ds_read2_b64 v[166:169], v214 offset0:42 offset1:50
	v_fma_f32 v176, -v151, v154, v134
	v_fma_f32 v177, -v151, v155, v135
	v_cndmask_b32_e64 v135, 0, 1.0, vcc
	v_cmp_eq_u32_e32 vcc, 6, v144
	v_mov_b32_e32 v154, v130
	v_mov_b32_e32 v155, v162
	v_mov_b32_e32 v162, v131
	v_mov_b32_e32 v164, v133
	s_waitcnt lgkmcnt(0)
	v_mov_b32_e32 v167, v172
	ds_read_b128 v[172:175], v179 offset:14848
	ds_read_b128 v[180:183], v179 offset:14864
	ds_read_b128 v[130:133], v179 offset:14944
	ds_read_b128 v[184:187], v179 offset:14976
	ds_read_b128 v[188:191], v179 offset:14912
	ds_read_b128 v[192:195], v179 offset:14928
	v_cndmask_b32_e64 v134, 0, 1.0, vcc
	v_fma_f32 v134, -v148, v154, v134
	v_fma_f32 v135, -v148, v155, v135
	v_cmp_eq_u32_e32 vcc, 10, v144
	v_mov_b32_e32 v149, v151
	ds_read_b128 v[196:199], v179 offset:14992
	ds_read_b128 v[200:203], v179 offset:15040
	s_waitcnt lgkmcnt(5)
	v_cndmask_b32_e64 v131, 0, 1.0, vcc
	s_waitcnt lgkmcnt(4)
	v_mul_f32_e32 v132, v148, v184
	v_mul_f32_e32 v133, v149, v185
	v_fma_f32 v162, -v151, v162, v134
	v_fma_f32 v163, -v151, v163, v135
	v_sub_f32_e32 v131, v131, v132
	v_sub_f32_e32 v131, v131, v133
	ds_read2_b64 v[132:135], v214 offset0:84 offset1:110
	v_cmp_eq_u32_e32 vcc, 11, v144
	v_mov_b32_e32 v152, v151
	s_waitcnt lgkmcnt(1)
	v_mov_b32_e32 v184, v201
	s_waitcnt lgkmcnt(0)
	v_cndmask_b32_e64 v135, 0, 1.0, vcc
	v_fma_f32 v154, -v148, v200, v135
	v_mov_b32_e32 v185, v151
	v_mov_b32_e32 v155, v150
	v_fma_f32 v152, -v152, v184, v154
	v_fma_f32 v153, -v153, v185, v155
	v_mov_b32_e32 v154, v151
	v_mov_b32_e32 v155, v153
	v_mul_f32_e32 v154, v158, v154
	v_mul_f32_e32 v155, v159, v155
	v_fma_f32 v158, -v153, v204, v176
	v_fma_f32 v159, -v153, v205, v177
	v_sub_f32_e32 v135, v147, v154
	v_sub_f32_e32 v154, v135, v155
	v_fma_f32 v156, -v154, v156, v158
	v_fma_f32 v157, -v154, v157, v159
	v_fma_f32 v158, -v153, v206, v162
	v_fma_f32 v159, -v153, v207, v163
	v_mov_b32_e32 v162, v153
	v_mov_b32_e32 v163, v154
	v_mov_b32_e32 v216, v168
	v_mov_b32_e32 v217, v166
	v_fma_f32 v158, -v154, v164, v158
	v_fma_f32 v159, -v154, v165, v159
	v_mul_f32_e32 v162, v162, v186
	v_mul_f32_e32 v163, v163, v187
	v_fma_f32 v158, -v216, v157, v158
	v_fma_f32 v159, -v217, v157, v159
	v_sub_f32_e32 v131, v131, v162
	v_sub_f32_e32 v131, v131, v163
	v_mov_b32_e32 v162, v157
	v_mov_b32_e32 v163, v159
	v_mul_f32_e32 v162, v162, v196
	v_mul_f32_e32 v163, v163, v197
	v_mov_b32_e32 v166, v171
	v_sub_f32_e32 v131, v131, v162
	v_sub_f32_e32 v131, v131, v163
	ds_read_b128 v[162:165], v179 offset:15056
	ds_read_b128 v[184:187], v179 offset:15072
	v_fma_f32 v135, -v157, v170, v156
	v_mov_b32_e32 v155, v157
	v_mov_b32_e32 v170, v203
	s_waitcnt lgkmcnt(1)
	v_mov_b32_e32 v171, v162
	v_fma_f32 v147, -v153, v202, v152
	v_mul_f32_e32 v170, v154, v170
	v_mul_f32_e32 v171, v155, v171
	v_mov_b32_e32 v168, v159
	v_sub_f32_e32 v147, v147, v170
	v_sub_f32_e32 v162, v147, v171
	v_mov_b32_e32 v170, v163
	v_mov_b32_e32 v171, v159
	v_mov_b32_e32 v163, v158
	v_fma_f32 v196, -v168, v170, v162
	v_fma_f32 v197, -v169, v171, v163
	v_mov_b32_e32 v162, v159
	v_mov_b32_e32 v163, v197
	v_mul_f32_e32 v162, v166, v162
	v_mul_f32_e32 v163, v167, v163
	v_mov_b32_e32 v200, v197
	v_sub_f32_e32 v135, v135, v162
	v_sub_f32_e32 v201, v135, v163
	v_mul_f32_e32 v162, v200, v198
	v_mul_f32_e32 v163, v201, v199
	v_cmp_eq_u32_e32 vcc, 8, v144
	v_sub_f32_e32 v131, v131, v162
	v_sub_f32_e32 v131, v131, v163
	v_cndmask_b32_e64 v163, 0, 1.0, vcc
	v_cmp_eq_u32_e32 vcc, 9, v144
	v_mov_b32_e32 v166, v188
	v_mov_b32_e32 v167, v172
	v_cndmask_b32_e64 v162, 0, 1.0, vcc
	v_fma_f32 v162, -v148, v166, v162
	v_fma_f32 v163, -v148, v167, v163
	v_mov_b32_e32 v172, v189
	v_fma_f32 v162, -v151, v172, v162
	v_fma_f32 v163, -v151, v173, v163
	v_mov_b32_e32 v166, v190
	v_mov_b32_e32 v167, v174
	v_fma_f32 v162, -v153, v166, v162
	v_fma_f32 v163, -v153, v167, v163
	v_mov_b32_e32 v174, v191
	v_fma_f32 v162, -v154, v174, v162
	v_fma_f32 v163, -v154, v175, v163
	v_mov_b32_e32 v166, v192
	v_mov_b32_e32 v167, v180
	v_fma_f32 v162, -v157, v166, v162
	v_fma_f32 v163, -v157, v167, v163
	v_mov_b32_e32 v180, v193
	v_fma_f32 v162, -v159, v180, v162
	v_fma_f32 v163, -v159, v181, v163
	v_mov_b32_e32 v166, v194
	v_mov_b32_e32 v167, v182
	v_fma_f32 v162, -v197, v166, v162
	v_fma_f32 v163, -v197, v167, v163
	v_mov_b32_e32 v182, v195
	v_mov_b32_e32 v188, v201
	v_fma_f32 v190, -v182, v188, v162
	v_fma_f32 v191, -v183, v188, v163
	v_fma_f32 v135, -v197, v164, v196
	v_fma_f32 v193, -v130, v191, v190
	v_mov_b32_e32 v192, v191
	v_mov_b32_e32 v162, v201
	v_mov_b32_e32 v163, v191
	v_mov_b32_e32 v164, v165
	s_waitcnt lgkmcnt(0)
	v_mov_b32_e32 v165, v184
	v_mul_f32_e32 v132, v132, v192
	v_mul_f32_e32 v133, v133, v193
	v_mul_f32_e32 v162, v162, v164
	v_mul_f32_e32 v163, v163, v165
	v_sub_f32_e32 v131, v131, v132
	v_sub_f32_e32 v132, v135, v162
	v_sub_f32_e32 v135, v132, v163
	v_sub_f32_e32 v133, v131, v133
	v_mov_b32_e32 v162, v185
	v_mov_b32_e32 v163, v186
	v_mov_b32_e32 v132, v193
	v_mul_f32_e32 v162, v162, v132
	v_mul_f32_e32 v163, v163, v133
	v_cmp_eq_u32_e32 vcc, 12, v144
	v_sub_f32_e32 v131, v135, v162
	v_sub_f32_e32 v192, v131, v163
	ds_read_b128 v[162:165], v179 offset:15328
	ds_read_b128 v[166:169], v179 offset:15344
	ds_read_b128 v[170:173], v179 offset:15104
	ds_read_b128 v[174:177], v179 offset:15120
	ds_read_b128 v[180:183], v179 offset:15136
	v_cndmask_b32_e64 v147, 0, 1.0, vcc
	v_mov_b32_e32 v184, v140
	s_waitcnt lgkmcnt(2)
	v_mov_b32_e32 v185, v170
	v_fma_f32 v146, -v148, v184, v146
	v_fma_f32 v147, -v148, v185, v147
	v_mov_b32_e32 v170, v141
	v_fma_f32 v140, -v151, v170, v146
	v_fma_f32 v141, -v151, v171, v147
	v_mov_b32_e32 v146, v142
	v_mov_b32_e32 v147, v172
	v_fma_f32 v140, -v146, v153, v140
	v_fma_f32 v141, -v147, v153, v141
	v_mov_b32_e32 v172, v143
	v_fma_f32 v140, -v172, v154, v140
	v_fma_f32 v141, -v173, v154, v141
	v_mov_b32_e32 v142, v136
	s_waitcnt lgkmcnt(1)
	v_mov_b32_e32 v143, v174
	v_fma_f32 v140, -v157, v142, v140
	v_fma_f32 v141, -v157, v143, v141
	v_mov_b32_e32 v174, v137
	v_fma_f32 v136, -v159, v174, v140
	v_fma_f32 v137, -v159, v175, v141
	v_mov_b32_e32 v140, v138
	v_mov_b32_e32 v141, v176
	v_fma_f32 v136, -v140, v197, v136
	v_fma_f32 v137, -v141, v197, v137
	v_mov_b32_e32 v176, v139
	v_fma_f32 v140, -v176, v188, v136
	v_fma_f32 v141, -v177, v188, v137
	v_mov_b32_e32 v142, v162
	s_waitcnt lgkmcnt(0)
	v_mov_b32_e32 v143, v180
	v_fma_f32 v140, -v142, v191, v140
	v_fma_f32 v141, -v143, v191, v141
	v_mov_b32_e32 v180, v163
	v_fma_f32 v140, -v180, v132, v140
	v_fma_f32 v141, -v181, v132, v141
	v_mov_b32_e32 v142, v164
	v_mov_b32_e32 v143, v182
	v_mov_b32_e32 v146, v133
	v_fma_f32 v140, -v142, v146, v140
	v_fma_f32 v141, -v143, v146, v141
	v_mov_b32_e32 v182, v165
	ds_read_b128 v[136:139], v179 offset:15168
	v_fma_f32 v194, -v182, v192, v140
	v_fma_f32 v195, -v183, v192, v141
	ds_read_b128 v[140:143], v179 offset:15184
	ds_read_b128 v[162:165], v179 offset:15200
	ds_read_b128 v[170:173], v179 offset:15232
	v_cmp_eq_u32_e32 vcc, 13, v144
	ds_read_b128 v[174:177], v179 offset:15248
	s_waitcnt lgkmcnt(4)
	v_mov_b32_e32 v183, v136
	v_cndmask_b32_e64 v181, 0, 1.0, vcc
	v_cmp_eq_u32_e32 vcc, 14, v144
	s_waitcnt lgkmcnt(1)
	v_mov_b32_e32 v182, v170
	v_mov_b32_e32 v136, v171
	v_cndmask_b32_e64 v180, 0, 1.0, vcc
	v_fma_f32 v198, -v148, v182, v180
	v_fma_f32 v199, -v148, v183, v181
	v_fma_f32 v136, -v151, v136, v198
	v_fma_f32 v137, -v151, v137, v199
	v_mov_b32_e32 v170, v172
	v_mov_b32_e32 v171, v138
	v_fma_f32 v136, -v153, v170, v136
	v_fma_f32 v137, -v153, v171, v137
	v_mov_b32_e32 v138, v173
	ds_read_b128 v[180:183], v179 offset:15264
	ds_read_b128 v[184:187], v179 offset:15280
	v_fma_f32 v136, -v154, v138, v136
	v_fma_f32 v137, -v154, v139, v137
	s_waitcnt lgkmcnt(2)
	v_mov_b32_e32 v138, v174
	v_mov_b32_e32 v139, v140
	v_fma_f32 v136, -v157, v138, v136
	v_fma_f32 v137, -v157, v139, v137
	v_mov_b32_e32 v140, v175
	v_fma_f32 v136, -v159, v140, v136
	v_fma_f32 v137, -v159, v141, v137
	v_mov_b32_e32 v138, v176
	v_mov_b32_e32 v139, v142
	v_fma_f32 v136, -v197, v138, v136
	v_fma_f32 v137, -v197, v139, v137
	v_mov_b32_e32 v142, v177
	v_fma_f32 v136, -v188, v142, v136
	v_fma_f32 v137, -v188, v143, v137
	s_waitcnt lgkmcnt(1)
	v_mov_b32_e32 v138, v180
	v_mov_b32_e32 v139, v162
	v_fma_f32 v136, -v191, v138, v136
	v_fma_f32 v137, -v191, v139, v137
	v_mov_b32_e32 v162, v181
	v_fma_f32 v136, -v132, v162, v136
	v_fma_f32 v137, -v132, v163, v137
	v_mov_b32_e32 v138, v182
	v_mov_b32_e32 v139, v164
	v_fma_f32 v136, -v146, v138, v136
	v_fma_f32 v137, -v146, v139, v137
	v_mov_b32_e32 v164, v183
	v_fma_f32 v136, -v192, v164, v136
	v_fma_f32 v137, -v192, v165, v137
	s_waitcnt lgkmcnt(0)
	v_mov_b32_e32 v138, v184
	v_mov_b32_e32 v139, v134
	v_fma_f32 v136, -v138, v195, v136
	v_fma_f32 v137, -v139, v195, v137
	v_mov_b32_e32 v138, v167
	v_fma_f32 v135, -v185, v137, v136
	v_mov_b32_e32 v139, v168
	v_mov_b32_e32 v134, v137
	v_cvt_f16_f32_e32 v132, v191
	v_fma_f32 v131, -v166, v195, v194
	v_mul_f32_e32 v138, v138, v134
	v_mul_f32_e32 v139, v139, v135
	v_cvt_pk_f16_f32 v134, v195, v137
	v_sub_f32_e32 v131, v131, v138
	v_sub_f32_e32 v131, v131, v139
	v_cvt_pk_f16_f32 v139, v197, v201
	v_cvt_pk_f16_f32 v138, v157, v159
	v_cvt_pk_f16_f32 v137, v153, v154
	v_cvt_pk_f16_f32 v136, v148, v151
	v_cvt_pk_f16_f32 v135, v135, v131
	v_cvt_pk_f16_f32 v133, v133, v192
	v_fma_mixhi_f16 v132, -v130, v191, v190
	ds_write_b128 v161, v[136:139] offset:15360
	ds_write_b128 v161, v[132:135] offset:15376
	s_branch .LBB0_1289
